# NSA tile loop: lane-mask tests on the scalar unit (on v17)
# baseline (speedup 1.0000x reference)
.LBB0_2436:
	s_and_b64 vcc, s[78:79], exec
	s_nop 0
	s_nop 0
	s_cmp_lg_u64 vcc, 0
	s_cselect_b64 s[80:81], -1, 0
	s_and_b32 s82, s2, 0x6000
	v_add_u32_e32 v224, s82, v182
	ds_read_b128 v[228:231], v224 offset:512
	ds_read_b128 v[232:235], v224 offset:2560
	ds_read_b128 v[236:239], v224 offset:4608
	ds_read_b128 v[240:243], v224 offset:6656
	s_waitcnt lgkmcnt(3)
	v_mfma_f32_32x32x16_bf16 v[82:97], v[228:231], v[114:117], v[34:49]
	s_waitcnt lgkmcnt(2)
	v_mfma_f32_32x32x16_bf16 v[82:97], v[232:235], v[118:121], v[82:97]
	s_waitcnt lgkmcnt(1)
	v_mfma_f32_32x32x16_bf16 v[82:97], v[236:239], v[122:125], v[82:97]
	s_waitcnt lgkmcnt(0)
	v_mfma_f32_32x32x16_bf16 v[82:97], v[240:243], v[126:129], v[82:97]
	ds_read_b64_tr_b16 v[228:229], v225
	ds_read_b64_tr_b16 v[230:231], v225 offset:512
	ds_read_b64_tr_b16 v[232:233], v225 offset:1024
	ds_read_b64_tr_b16 v[234:235], v225 offset:1536
	ds_read_b64_tr_b16 v[236:237], v225 offset:4096
	ds_read_b64_tr_b16 v[238:239], v225 offset:4608
	ds_read_b64_tr_b16 v[240:241], v225 offset:5120
	ds_read_b64_tr_b16 v[242:243], v225 offset:5632
	s_cbranch_vccz .LBB0_2438
	v_cndmask_b32_e64 v50, v50, v1, s[78:79]
	v_cndmask_b32_e64 v51, v51, v1, s[78:79]
	v_cndmask_b32_e64 v52, v52, v1, s[78:79]
	v_cndmask_b32_e64 v53, v53, v1, s[78:79]
	v_cndmask_b32_e64 v54, v54, v1, s[78:79]
	v_cndmask_b32_e64 v55, v55, v1, s[78:79]
	v_cndmask_b32_e64 v56, v56, v1, s[78:79]
	v_cndmask_b32_e64 v57, v57, v1, s[78:79]
	v_cndmask_b32_e64 v58, v58, v1, s[78:79]
	v_cndmask_b32_e64 v59, v59, v1, s[78:79]
	v_cndmask_b32_e64 v60, v60, v1, s[78:79]
	v_cndmask_b32_e64 v61, v61, v1, s[78:79]
	v_cndmask_b32_e64 v62, v62, v1, s[78:79]
	v_cndmask_b32_e64 v63, v63, v1, s[78:79]
	v_cndmask_b32_e64 v64, v64, v1, s[78:79]
	v_cndmask_b32_e64 v65, v65, v1, s[78:79]
.LBB0_2438:
	s_and_b64 s[82:83], exec, s[72:73]
	s_cselect_b32 s82, s93, 0
	s_sub_i32 s82, s92, s82
	s_add_i32 s84, s82, -8
	s_cmp_lg_u32 s82, s3
	s_cselect_b64 s[82:83], -1, 0
	s_cmp_eq_u32 s84, s3
	s_cselect_b64 s[84:85], -1, 0
	s_and_b64 s[72:73], s[72:73], s[84:85]
	s_andn2_b64 s[72:73], exec, s[72:73]
	s_nop 0
	s_mov_b64 s[84:85], -1
	s_and_b64 vcc, exec, s[82:83]
	s_nop 0
	s_nop 0
	s_cbranch_vccz .LBB0_2442
	s_and_b64 vcc, exec, s[72:73]
	s_cbranch_vccnz .LBB0_2441
	v_cndmask_b32_e64 v50, v1, v50, s[6:7]
	v_cndmask_b32_e64 v51, v51, v1, s[8:9]
	v_cndmask_b32_e64 v52, v1, v52, s[10:11]
	v_cndmask_b32_e64 v53, v1, v53, s[12:13]
	v_cndmask_b32_e64 v54, v1, v54, s[14:15]
	v_cndmask_b32_e64 v55, v1, v55, s[16:17]
	v_cndmask_b32_e64 v56, v1, v56, s[18:19]
	v_cndmask_b32_e64 v57, v1, v57, s[20:21]
	v_cndmask_b32_e64 v58, v1, v58, s[22:23]
	v_cndmask_b32_e64 v59, v1, v59, s[24:25]
	v_cndmask_b32_e64 v60, v1, v60, s[26:27]
	v_cndmask_b32_e64 v61, v1, v61, s[28:29]
	v_cndmask_b32_e64 v62, v1, v62, s[30:31]
	v_cndmask_b32_e64 v63, v1, v63, s[34:35]
	v_cndmask_b32_e64 v64, v1, v64, s[36:37]
	v_cndmask_b32_e64 v65, v1, v65, s[38:39]
